# phase A: workgroups with bit 3 of their index set run the in-projection GEMM before the expert-weight conversion (others convert first), so HBM-bound and matrix-bound work overlap
# speedup vs baseline: 1.0036x; 1.0036x over previous
; #define LAS __attribute__((address_space(3)))
; #define REP(k) for (int _rep = 0; _rep < (((PROBE_MASK >> (k)) & 1) ? 2 : 1); ++_rep)
; __device__ __forceinline__ void p_expert_weights(Frame& F, int l, int it0, int it1, int nw, int w) {
;     LAS float* scr = (LAS float*)(F.lds + F.wave * 16384);
;     constexpr int I1 = 16 * 8, I2 = 4 * 32, PER_E = 2 * I1 + I2;
;     for (int it = it0 + w; it < it1; it += nw) {
; __global__ void __launch_bounds__(NTHR, 2) mk_fwd(Args args) {
;     ...
;             REP(0) { p_expert_weights(F, l, (last || F.G != 256) ? 0 : XW_TAIL_G, XW_ITEMS, F.G * NWAVES, F.wg * NWAVES + F.wave); __syncthreads(); }
.LBB0_267:
	s_andn2_b64 vcc, exec, s[2:3]
	s_cbranch_vccnz .LBB0_381
	s_bitcmp1_b32 s96, 3
	s_cselect_b32 s100, 1, 0
.Lpa_body:
	v_readlane_b32 s36, v252, 8
	v_readlane_b32 s37, v252, 9
	s_mov_b32 s20, s97
	v_readlane_b32 s38, v252, 10
	v_readlane_b32 s39, v252, 11
	s_mov_b64 s[2:3], s[36:37]
	s_waitcnt vmcnt(0)
	v_mbcnt_lo_u32_b32 v6, -1, 0
	v_mbcnt_hi_u32_b32 v6, -1, v6
	s_nop 0
	v_readlane_b32 s2, v255, 30
	v_readlane_b32 s3, v255, 31
	s_or_b64 s[2:3], s[12:13], s[2:3]
	s_and_b64 s[2:3], s[2:3], exec
	s_cselect_b32 s0, 0, 0x4e00
	v_readlane_b32 s2, v254, 28
	s_add_i32 s0, s0, s2
	s_add_i32 s21, s0, s20
	s_cmp_eq_u32 s100, 1
	s_cselect_b32 s21, 0x10000, s21
	s_cmp_gt_i32 s21, 0xc17f
	s_cbranch_scc1 .LBB0_279
	s_lshl_b32 s0, s20, 14
	s_mov_b32 s31, s23
	s_add_i32 s0, s0, 0
	s_lshl_b64 s[2:3], s[30:31], 20
	s_lshl_b64 s[40:41], s[30:31], 27
	s_add_u32 s50, s38, 0x5900000
	s_addc_u32 s51, s39, 0
	s_add_u32 s52, s38, 0xda00000
	v_readlane_b32 s56, v252, 16
	s_addc_u32 s53, s39, 0
	v_readlane_b32 s57, v252, 17
	v_readlane_b32 s58, v252, 18
	v_readlane_b32 s59, v252, 19
	v_readlane_b32 s60, v252, 20
	v_readlane_b32 s61, v252, 21
	v_readlane_b32 s62, v252, 22
	v_readlane_b32 s63, v252, 23
	v_readlane_b32 s68, v252, 28
	v_lshlrev_b32_e32 v3, 5, v6
	v_readlane_b32 s69, v252, 29
	s_add_u32 s54, s68, s40
	v_readlane_b32 s56, v252, 0
	v_ashrrev_i32_e32 v7, 5, v6
	v_and_b32_e32 v0, 31, v6
	s_movk_i32 s4, 0x84
	v_ashrrev_i32_e32 v8, 1, v6
	v_and_b32_e32 v4, 32, v3
	s_addc_u32 s55, s69, s41
	v_readlane_b32 s58, v252, 2
	v_lshl_add_u32 v1, v0, 2, s0
	v_mul_lo_u32 v2, v7, s4
	v_mul_u32_u24_e32 v3, 0x84, v4
	v_lshlrev_b32_e32 v5, 2, v8
	v_readlane_b32 s57, v252, 1
	v_readlane_b32 s59, v252, 3
	v_readlane_b32 s60, v252, 4
	v_readlane_b32 s61, v252, 5
	s_add_u32 s56, s58, s2
	s_waitcnt lgkmcnt(0)
	v_add3_u32 v9, s0, v3, v5
	v_readlane_b32 s4, v255, 14
	v_add_u32_e32 v10, v1, v2
	s_addc_u32 s57, s59, s3
	v_mov_b32_e32 v5, v193
	s_lshl_b32 s58, s21, 5
	s_lshl_b32 s59, s4, 5
	s_lshl_b32 s60, s21, 1
	s_lshl_b32 s61, s4, 1
	v_lshlrev_b32_e32 v192, 2, v0
	v_add_u32_e32 v11, 0x400, v10
	v_add_u32_e32 v12, 0x800, v10
	v_add_u32_e32 v13, 0xc00, v10
	v_add_u32_e32 v14, 0x1000, v10
	v_add_u32_e32 v15, 0x1400, v10
	v_add_u32_e32 v16, 0x1800, v10
	v_add_u32_e32 v17, 0x1c00, v10
	v_add_u32_e32 v18, 0x400, v9
	v_add_u32_e32 v19, 0x800, v9
	v_add_u32_e32 v20, 0xc00, v9
	v_readlane_b32 s64, v252, 24
	v_readlane_b32 s65, v252, 25
	v_readlane_b32 s66, v252, 26
	v_readlane_b32 s67, v252, 27
	v_readlane_b32 s70, v252, 30
	v_readlane_b32 s71, v252, 31
	v_readlane_b32 s62, v252, 6
	v_readlane_b32 s63, v252, 7
	v_readlane_b32 s5, v255, 15
	s_branch .LBB0_272

; #define PG8_WAIT_V(n) asm volatile("s_waitcnt vmcnt(" #n ")" ::: "memory")
; template <class Epi, class Sched, bool GATHER, bool F8 = false, bool ALIGN_EPI = true, bool SP2 = true, bool NHALF = false, bool SWAP = false> ...
;     ...
;     const int tid = tid_, wid = __builtin_amdgcn_readfirstlane(tid >> 6), lane = tid & 63, wr = wid >> 2, wc = wid & 3, fr = lane & 15, fq = lane >> 4;
;     const int KB = F8 ? K : 2 * K;
;     const int nt = KB / 128;
;     unsigned voffB[2];
; #pragma unroll
;     for (int i = 0; i < 2; ++i) { int R, C; stage_rc(tid * 16 + i * 8192, R, C); const int Rb = Epi::PERM ? ((R & ~31) + perm32(R & 31)) : R;
;         voffB[i] = (unsigned)(Rb * KB + C * 2); }
;     const size_t kstep = (size_t)128;
;     const size_t hstep = (size_t)HALF * KB;
;     const unsigned ldsw = (unsigned)wid * 1024u;
;     const int aoff = F8 ? lds_byte(wr * 64 + fr, 16 * fq) : lds_byte(wr * 64 + fr, fq * 8), boff = F8 ? lds_byte(wc * 32 + fr, 16 * fq) : lds_byte(wc * 32 + fr, fq * 8);
;     constexpr int PIECE1 = F8 ? 16 : 1024;
;     const int sc_w = Epi::SCW, sc_a = 0x7F7F7F7F;
;     ...
;     static_assert(SP2, "only the two-super-phase K-loop is kept");
;     Unit cur, nxt; int ui = 0;
;     if (!S.next(0, cur)) return;
;     f32x4 acc[2][2][4][2];
; #pragma unroll
;     for (int a = 0; a < 2; ++a)
; #pragma unroll
;         for (int b = 0; b < 2; ++b)
; #pragma unroll
;             for (int m = 0; m < 4; ++m)
; #pragma unroll
;                 for (int n = 0; n < 2; ++n) acc[a][b][m][n] = (f32x4){0.f, 0.f, 0.f, 0.f};
;     bf16x8 At[F8 ? 1 : 4][2], B0[F8 ? 1 : 2][2], B1[F8 ? 1 : 2][2];
;     v8i At8[F8 ? 4 : 1], B08[F8 ? 2 : 1], B18[F8 ? 2 : 1];
;     unsigned ac[GATHER ? 2 : 1][2];
;     if (GATHER) { PG8_TABLOAD(0, cur.arow0); PG8_WAIT_V(0); PG8_BAR; }
;     PG8_AOFF_H(0, 0); if (GATHER) { PG8_AOFF_H((GATHER ? 1 : 0), 0); }
;     const char* cA = (const char*)Ag + (GATHER ? (size_t)0 : (size_t)cur.arow0 * KB); const char* cB = (const char*)Bg + (size_t)cur.brow0 * KB;
;     PG8_STAGE_B(PG8_SB(0, 0), cB); if constexpr (!NHALF) PG8_STAGE_B(PG8_SB(0, 1), cB + hstep); PG8_STAGE_A(PG8_SA(0, 0), cA, 0); PG8_STAGE_A(PG8_SA(0, 1), cA, 1);
;     if (wr == 1) PG8_BAR;
;     PG8_WAIT_V(2); PG8_BAR;
;     PG8_STAGE_B(PG8_SB(1, 0), cB + kstep); PG8_STAGE_A(PG8_SA(1, 0), cA + kstep, 0); if constexpr (!NHALF) PG8_STAGE_B(PG8_SB(1, 1), cB + hstep + kstep);
.LBB0_279:
	v_readlane_b32 s2, v253, 2
	v_lshl_or_b32 v10, s20, 6, v6
	v_readlane_b32 s3, v253, 3
	s_waitcnt lgkmcnt(0)
	s_barrier
	s_mul_i32 s22, s30, 0x340000
	s_cmp_eq_u32 s100, 2
	s_cselect_b64 s[2:3], 0, s[2:3]
	s_andn2_b64 vcc, exec, s[2:3]
	v_readfirstlane_b32 s2, v10
	s_cbranch_vccnz .LBB0_303
	v_lshlrev_b32_e32 v0, 4, v10
	v_add_u32_e32 v1, 0x2000, v0
	v_ashrrev_i32_e32 v2, 31, v1
	v_lshrrev_b32_e32 v2, 22, v2
	v_add_u32_e32 v2, v1, v2
	v_ashrrev_i32_e32 v2, 10, v2
	v_mul_i32_i24_e32 v3, 0x400, v2
	v_sub_u32_e32 v1, v1, v3
	v_lshrrev_b32_e32 v3, 4, v1
	v_bitop3_b32 v1, v3, v1, 32 bitop3:0x6c
	v_ashrrev_i32_e32 v3, 31, v1
	s_add_u32 s20, s38, 0x11b00000
	v_lshrrev_b32_e32 v3, 26, v3
	s_addc_u32 s21, s39, 0
	s_lshl_b64 s[4:5], s[22:23], 1
	v_add_u32_e32 v3, v1, v3
	v_lshlrev_b32_e32 v5, 3, v2
	s_add_u32 s0, s38, s4
	v_ashrrev_i32_e32 v4, 6, v3
	v_and_b32_e32 v5, -16, v5
	v_and_b32_e32 v3, 0xc0, v3
	s_addc_u32 s3, s39, s5
	v_add_u32_e32 v5, v4, v5
	v_and_b32_e32 v4, 3, v4
	s_mov_b32 s5, 0x1fffe0
	v_sub_u32_e32 v1, v1, v3
	v_and_or_b32 v4, v5, s5, v4
	v_lshrrev_b32_e32 v6, 2, v5
	v_lshlrev_b32_e32 v5, 1, v5
	v_lshlrev_b32_e32 v2, 5, v2
	v_ashrrev_i16_sdwa v1, v226, sext(v1) dst_sel:DWORD dst_unused:UNUSED_PAD src0_sel:DWORD src1_sel:BYTE_0
	v_and_b32_e32 v6, 4, v6
	v_and_b32_e32 v5, 24, v5
	v_and_b32_e32 v2, 32, v2
	v_bfe_i32 v1, v1, 0, 16
	v_or3_b32 v4, v4, v6, v5
	v_add_lshl_u32 v1, v2, v1, 1
	v_lshl_add_u32 v194, v4, 11, v1
	v_bfe_i32 v1, v10, 27, 1
	v_lshrrev_b32_e32 v1, 22, v1
	v_add_u32_e32 v1, v0, v1
	v_and_b32_e32 v1, 0xfffffc00, v1
	v_sub_u32_e32 v0, v0, v1
	v_lshrrev_b32_e32 v1, 4, v0
	v_ashrrev_i32_e32 v3, 31, v10
	v_bitop3_b32 v0, v1, v0, 32 bitop3:0x6c
	v_lshrrev_b32_e32 v3, 26, v3
	v_ashrrev_i32_e32 v1, 31, v0
	v_add_u32_e32 v3, v10, v3
	v_lshrrev_b32_e32 v1, 26, v1
	v_ashrrev_i32_e32 v3, 6, v3
	v_add_u32_e32 v1, v0, v1
	v_lshlrev_b32_e32 v4, 3, v3
	v_ashrrev_i32_e32 v2, 6, v1
	v_and_b32_e32 v4, -16, v4
	v_and_b32_e32 v1, 0xc0, v1
	v_add_u32_e32 v4, v2, v4
	v_and_b32_e32 v2, 3, v2
	v_sub_u32_e32 v0, v0, v1
	v_and_or_b32 v2, v4, s5, v2
	v_lshrrev_b32_e32 v5, 2, v4
	v_lshlrev_b32_e32 v4, 1, v4
	v_lshlrev_b32_e32 v3, 5, v3
	v_ashrrev_i16_sdwa v0, v226, sext(v0) dst_sel:DWORD dst_unused:UNUSED_PAD src0_sel:DWORD src1_sel:BYTE_0
	v_and_b32_e32 v5, 4, v5
	v_and_b32_e32 v4, 24, v4
	v_and_b32_e32 v3, 32, v3
	v_bfe_i32 v0, v0, 0, 16
	v_or3_b32 v2, v2, v5, v4
	v_add_lshl_u32 v0, v3, v0, 1
	v_lshl_add_u32 v192, v2, 11, v0
	v_mov_b32_e32 v0, v10
	s_add_u32 s64, s0, 0x300000
	v_ashrrev_i32_e32 v2, 31, v0
	v_lshrrev_b32_e32 v2, 26, v2
	v_lshlrev_b32_e32 v1, 4, v0
	v_add_u32_e32 v2, v0, v2
	v_bfe_i32 v0, v0, 27, 1
	v_lshrrev_b32_e32 v0, 22, v0
	v_add_u32_e32 v0, v1, v0
	v_and_b32_e32 v0, 0xfffffc00, v0
	v_sub_u32_e32 v0, v1, v0
	v_ashrrev_i32_e32 v8, 6, v2
	v_lshrrev_b32_e32 v2, 4, v0
	v_bitop3_b32 v0, v2, v0, 32 bitop3:0x6c
	v_ashrrev_i32_e32 v3, 31, v0
	v_lshrrev_b32_e32 v3, 26, v3
	v_add_u32_e32 v3, v0, v3
	v_ashrrev_i32_e32 v9, 6, v3
	v_and_b32_e32 v3, 0xc0, v3
	v_sub_u32_e32 v0, v0, v3
	v_lshlrev_b32_e32 v2, 3, v8
	v_lshlrev_b32_e32 v4, 5, v8
	v_ashrrev_i16_sdwa v0, v226, sext(v0) dst_sel:DWORD dst_unused:UNUSED_PAD src0_sel:DWORD src1_sel:BYTE_0
	v_and_b32_e32 v2, 0x1ffff0, v2
	v_and_b32_e32 v4, 32, v4
	v_bfe_i32 v11, v0, 0, 16
	v_add_u32_e32 v0, v4, v11
	v_add_lshl_u32 v2, v9, v2, 11
	v_lshl_add_u32 v196, v0, 1, v2
	v_add_u32_e32 v0, 0x2000, v1
	v_ashrrev_i32_e32 v1, 31, v0
	v_lshrrev_b32_e32 v1, 22, v1
	v_add_u32_e32 v1, v0, v1
	v_ashrrev_i32_e32 v12, 10, v1
	v_mul_i32_i24_e32 v1, 0x400, v12
	v_sub_u32_e32 v0, v0, v1
	s_addc_u32 s65, s3, 0
	s_ashr_i32 s3, s2, 6
	v_lshrrev_b32_e32 v1, 4, v0
	s_ashr_i32 s4, s2, 8
	s_lshl_b32 s0, s3, 10
	v_bitop3_b32 v0, v1, v0, 32 bitop3:0x6c
	v_readlane_b32 s5, v254, 47
	v_ashrrev_i32_e32 v2, 31, v0
	s_add_u32 s56, s64, s5
	v_lshrrev_b32_e32 v2, 26, v2
	s_addc_u32 s57, s65, 0
	s_add_i32 s66, s0, 0
	v_add_u32_e32 v2, v0, v2
	s_add_i32 s67, s66, 0x10000
	s_add_i32 s68, s66, 0x12000
	v_ashrrev_i32_e32 v13, 6, v2
	v_and_b32_e32 v2, 0xc0, v2
	s_mov_b32 m0, s67
	s_add_u32 s18, s56, 0x40000
	v_sub_u32_e32 v0, v0, v2
	global_load_lds_dwordx4 v192, s[56:57]
	s_mov_b32 m0, s68
	s_addc_u32 s19, s57, 0
	s_add_i32 s69, s66, 0x14000
	s_add_i32 s70, s66, 0x16000
	v_readlane_b32 s8, v254, 44
	v_lshlrev_b32_e32 v1, 3, v12
	v_lshlrev_b32_e32 v3, 5, v12
	v_ashrrev_i16_sdwa v0, v226, sext(v0) dst_sel:DWORD dst_unused:UNUSED_PAD src0_sel:DWORD src1_sel:BYTE_0
	global_load_lds_dwordx4 v194, s[56:57]
	s_mov_b32 m0, s69
	v_readlane_b32 s9, v254, 45
	s_add_u32 s44, s20, s8
	v_and_b32_e32 v1, 0x1ffff0, v1
	v_and_b32_e32 v3, 32, v3
	v_bfe_i32 v14, v0, 0, 16
	global_load_lds_dwordx4 v192, s[18:19]
	s_mov_b32 m0, s70
	s_addc_u32 s45, s21, s9
	s_add_i32 s71, s66, 0x2000
	v_add_u32_e32 v0, v3, v14
	v_add_lshl_u32 v1, v13, v1, 11
	global_load_lds_dwordx4 v194, s[18:19]
	s_mov_b32 m0, s66
	s_add_u32 s18, s44, 0x40000
	v_lshl_add_u32 v198, v0, 1, v1
	global_load_lds_dwordx4 v196, s[44:45]
	s_mov_b32 m0, s71
	s_addc_u32 s19, s45, 0
	s_add_i32 s72, s66, 0x4000
	global_load_lds_dwordx4 v198, s[44:45]
	s_mov_b32 m0, s72
	s_add_i32 s73, s66, 0x6000
	global_load_lds_dwordx4 v196, s[18:19]
	s_mov_b32 m0, s73
	v_mov_b32_e32 v195, v193
	global_load_lds_dwordx4 v198, s[18:19]
	v_mov_b32_e32 v197, v193
	v_mov_b32_e32 v199, v193
	s_cmp_eq_u32 s4, 1
	v_lshl_add_u64 v[6:7], s[56:57], 0, v[192:193]
	v_lshl_add_u64 v[4:5], s[56:57], 0, v[194:195]
	v_lshl_add_u64 v[0:1], s[44:45], 0, v[196:197]
	s_cselect_b64 s[40:41], -1, 0
	s_cmp_lg_u32 s4, 1
	v_lshl_add_u64 v[2:3], s[44:45], 0, v[198:199]
	s_cbranch_scc1 .LBB0_282
	s_barrier

; #define PG8_WAIT_V(n) asm volatile("s_waitcnt vmcnt(" #n ")" ::: "memory")
; template <class Epi, class Sched, bool GATHER, bool F8 = false, bool ALIGN_EPI = true, bool SP2 = true, bool NHALF = false, bool SWAP = false> ...
;     ...
;     const int tid = tid_, wid = __builtin_amdgcn_readfirstlane(tid >> 6), lane = tid & 63, wr = wid >> 2, wc = wid & 3, fr = lane & 15, fq = lane >> 4;
;     const int KB = F8 ? K : 2 * K;
;     const int nt = KB / 128;
;     unsigned voffB[2];
; #pragma unroll
;     for (int i = 0; i < 2; ++i) { int R, C; stage_rc(tid * 16 + i * 8192, R, C); const int Rb = Epi::PERM ? ((R & ~31) + perm32(R & 31)) : R;
;         voffB[i] = (unsigned)(Rb * KB + C * 2); }
;     const size_t kstep = (size_t)128;
;     const size_t hstep = (size_t)HALF * KB;
;     const unsigned ldsw = (unsigned)wid * 1024u;
;     const int aoff = F8 ? lds_byte(wr * 64 + fr, 16 * fq) : lds_byte(wr * 64 + fr, fq * 8), boff = F8 ? lds_byte(wc * 32 + fr, 16 * fq) : lds_byte(wc * 32 + fr, fq * 8);
;     constexpr int PIECE1 = F8 ? 16 : 1024;
;     const int sc_w = Epi::SCW, sc_a = 0x7F7F7F7F;
;     ...
;     static_assert(SP2, "only the two-super-phase K-loop is kept");
;     Unit cur, nxt; int ui = 0;
;     if (!S.next(0, cur)) return;
;     f32x4 acc[2][2][4][2];
; #pragma unroll
;     for (int a = 0; a < 2; ++a)
; #pragma unroll
;         for (int b = 0; b < 2; ++b)
; #pragma unroll
;             for (int m = 0; m < 4; ++m)
; #pragma unroll
;                 for (int n = 0; n < 2; ++n) acc[a][b][m][n] = (f32x4){0.f, 0.f, 0.f, 0.f};
;     bf16x8 At[F8 ? 1 : 4][2], B0[F8 ? 1 : 2][2], B1[F8 ? 1 : 2][2];
;     v8i At8[F8 ? 4 : 1], B08[F8 ? 2 : 1], B18[F8 ? 2 : 1];
;     unsigned ac[GATHER ? 2 : 1][2];
;     if (GATHER) { PG8_TABLOAD(0, cur.arow0); PG8_WAIT_V(0); PG8_BAR; }
;     PG8_AOFF_H(0, 0); if (GATHER) { PG8_AOFF_H((GATHER ? 1 : 0), 0); }
;     const char* cA = (const char*)Ag + (GATHER ? (size_t)0 : (size_t)cur.arow0 * KB); const char* cB = (const char*)Bg + (size_t)cur.brow0 * KB;
;     PG8_STAGE_B(PG8_SB(0, 0), cB); if constexpr (!NHALF) PG8_STAGE_B(PG8_SB(0, 1), cB + hstep); PG8_STAGE_A(PG8_SA(0, 0), cA, 0); PG8_STAGE_A(PG8_SA(0, 1), cA, 1);
;     if (wr == 1) PG8_BAR;
;     PG8_WAIT_V(2); PG8_BAR;
;     PG8_STAGE_B(PG8_SB(1, 0), cB + kstep); PG8_STAGE_A(PG8_SA(1, 0), cA + kstep, 0); if constexpr (!NHALF) PG8_STAGE_B(PG8_SB(1, 1), cB + hstep + kstep);
.LBB0_303:
	v_readlane_b32 s36, v252, 8
	v_readlane_b32 s37, v252, 9
	v_readlane_b32 s38, v252, 10
	v_readlane_b32 s39, v252, 11
	s_mov_b32 s0, s97
	s_mov_b64 s[2:3], s[38:39]
	s_mov_b64 s[4:5], s[36:37]
	s_waitcnt vmcnt(0)
	s_barrier
	v_mbcnt_lo_u32_b32 v0, -1, 0
	v_mbcnt_hi_u32_b32 v0, -1, v0
	s_nop 0
	v_readlane_b32 s4, v254, 50
	v_lshl_or_b32 v8, s0, 6, v0
	v_readlane_b32 s5, v254, 51
	s_cmp_eq_u32 s100, 2
	s_cselect_b64 s[4:5], 0, s[4:5]
	s_andn2_b64 vcc, exec, s[4:5]
	v_readfirstlane_b32 s4, v8
	s_cbranch_vccnz .LBB0_331
	v_lshlrev_b32_e32 v0, 4, v8
	v_add_u32_e32 v1, 0x2000, v0
	v_ashrrev_i32_e32 v2, 31, v1
	v_lshrrev_b32_e32 v2, 22, v2
	v_add_u32_e32 v2, v1, v2
	v_ashrrev_i32_e32 v2, 10, v2
	v_mul_i32_i24_e32 v4, 0x400, v2
	v_sub_u32_e32 v1, v1, v4
	v_lshrrev_b32_e32 v4, 4, v1
	v_bitop3_b32 v1, v4, v1, 32 bitop3:0x6c
	v_ashrrev_i32_e32 v4, 31, v1
	v_lshrrev_b32_e32 v4, 26, v4
	v_add_u32_e32 v4, v1, v4
	v_lshrrev_b32_e32 v5, 6, v4
	v_and_b32_e32 v4, 0xc0, v4
	v_lshlrev_b32_e32 v3, 5, v2
	v_sub_u32_e32 v1, v1, v4
	v_and_b32_e32 v3, 32, v3
	v_ashrrev_i16_sdwa v1, v226, sext(v1) dst_sel:DWORD dst_unused:UNUSED_PAD src0_sel:DWORD src1_sel:BYTE_0
	v_add_u32_sdwa v1, v3, sext(v1) dst_sel:DWORD dst_unused:UNUSED_PAD src0_sel:DWORD src1_sel:WORD_0
	v_bfe_i32 v3, v8, 27, 1
	v_lshrrev_b32_e32 v3, 22, v3
	v_add_u32_e32 v3, v0, v3
	v_and_b32_e32 v3, 0xfffffc00, v3
	v_lshlrev_b32_e32 v2, 3, v2
	v_sub_u32_e32 v0, v0, v3
	v_and_b32_e32 v2, 0x1ffff0, v2
	v_lshrrev_b32_e32 v3, 4, v0
	v_add_lshl_u32 v2, v5, v2, 11
	v_bitop3_b32 v0, v3, v0, 32 bitop3:0x6c
	v_lshl_add_u32 v194, v1, 1, v2
	v_ashrrev_i32_e32 v1, 31, v8
	v_ashrrev_i32_e32 v3, 31, v0
	v_lshrrev_b32_e32 v1, 26, v1
	v_lshrrev_b32_e32 v3, 26, v3
	v_add_u32_e32 v1, v8, v1
	v_add_u32_e32 v3, v0, v3
	v_ashrrev_i32_e32 v1, 6, v1
	v_lshrrev_b32_e32 v4, 6, v3
	v_and_b32_e32 v3, 0xc0, v3
	v_lshlrev_b32_e32 v2, 5, v1
	v_sub_u32_e32 v0, v0, v3
	v_lshlrev_b32_e32 v1, 3, v1
	v_and_b32_e32 v2, 32, v2
	v_ashrrev_i16_sdwa v0, v226, sext(v0) dst_sel:DWORD dst_unused:UNUSED_PAD src0_sel:DWORD src1_sel:BYTE_0
	v_and_b32_e32 v1, 0x1ffff0, v1
	v_add_u32_sdwa v0, v2, sext(v0) dst_sel:DWORD dst_unused:UNUSED_PAD src0_sel:DWORD src1_sel:WORD_0
	v_add_lshl_u32 v1, v4, v1, 11
	v_lshl_add_u32 v196, v0, 1, v1
	v_mov_b32_e32 v0, v8
	s_add_u32 s20, s2, 0x11b00000
	v_ashrrev_i32_e32 v2, 31, v0
	v_lshrrev_b32_e32 v2, 26, v2
	v_lshlrev_b32_e32 v1, 4, v0
	v_add_u32_e32 v2, v0, v2
	v_bfe_i32 v0, v0, 27, 1
	v_lshrrev_b32_e32 v0, 22, v0
	v_add_u32_e32 v0, v1, v0
	v_and_b32_e32 v0, 0xfffffc00, v0
	v_sub_u32_e32 v0, v1, v0
	v_ashrrev_i32_e32 v9, 6, v2
	v_lshrrev_b32_e32 v2, 4, v0
	v_bitop3_b32 v0, v2, v0, 32 bitop3:0x6c
	v_ashrrev_i32_e32 v3, 31, v0
	v_lshrrev_b32_e32 v3, 26, v3
	v_add_u32_e32 v3, v0, v3
	v_ashrrev_i32_e32 v10, 6, v3
	v_and_b32_e32 v3, 0xc0, v3
	v_sub_u32_e32 v0, v0, v3
	v_lshlrev_b32_e32 v2, 3, v9
	v_lshlrev_b32_e32 v4, 5, v9
	v_ashrrev_i16_sdwa v0, v226, sext(v0) dst_sel:DWORD dst_unused:UNUSED_PAD src0_sel:DWORD src1_sel:BYTE_0
	v_and_b32_e32 v2, 0x1ffff0, v2
	v_and_b32_e32 v4, 32, v4
	v_bfe_i32 v11, v0, 0, 16
	v_add_u32_e32 v0, v4, v11
	v_add_lshl_u32 v2, v10, v2, 11
	v_lshl_add_u32 v198, v0, 1, v2
	v_add_u32_e32 v0, 0x2000, v1
	v_ashrrev_i32_e32 v1, 31, v0
	v_lshrrev_b32_e32 v1, 22, v1
	s_addc_u32 s21, s3, 0
	s_lshl_b64 s[18:19], s[22:23], 1
	v_add_u32_e32 v1, v0, v1
	s_add_u32 s0, s2, s18
	v_ashrrev_i32_e32 v12, 10, v1
	s_addc_u32 s5, s3, s19
	v_mul_i32_i24_e32 v1, 0x400, v12
	s_add_u32 s66, s0, 0x300000
	v_sub_u32_e32 v0, v0, v1
	s_addc_u32 s67, s5, 0
	s_ashr_i32 s5, s4, 6
	v_lshrrev_b32_e32 v1, 4, v0
	s_ashr_i32 s18, s4, 8
	s_lshl_b32 s0, s5, 10
	v_bitop3_b32 v0, v1, v0, 32 bitop3:0x6c
	v_readlane_b32 s8, v254, 59
	v_ashrrev_i32_e32 v2, 31, v0
	s_add_u32 s38, s66, s8
	v_lshrrev_b32_e32 v2, 26, v2
	s_addc_u32 s39, s67, 0
	s_add_i32 s68, s0, 0
	v_add_u32_e32 v2, v0, v2
	s_add_i32 s69, s68, 0x10000
	s_add_i32 s70, s68, 0x12000
	v_ashrrev_i32_e32 v13, 6, v2
	v_and_b32_e32 v2, 0xc0, v2
	s_mov_b32 m0, s69
	s_add_u32 s36, s38, 0x40000
	v_sub_u32_e32 v0, v0, v2
	global_load_lds_dwordx4 v196, s[38:39]
	s_mov_b32 m0, s70
	s_addc_u32 s37, s39, 0
	s_add_i32 s71, s68, 0x14000
	s_add_i32 s72, s68, 0x16000
	v_readlane_b32 s8, v254, 56
	v_lshlrev_b32_e32 v1, 3, v12
	v_lshlrev_b32_e32 v3, 5, v12
	v_ashrrev_i16_sdwa v0, v226, sext(v0) dst_sel:DWORD dst_unused:UNUSED_PAD src0_sel:DWORD src1_sel:BYTE_0
	global_load_lds_dwordx4 v194, s[38:39]
	s_mov_b32 m0, s71
	v_readlane_b32 s9, v254, 57
	s_add_u32 s54, s20, s8
	v_and_b32_e32 v1, 0x1ffff0, v1
	v_and_b32_e32 v3, 32, v3
	v_bfe_i32 v14, v0, 0, 16
	global_load_lds_dwordx4 v196, s[36:37]
	s_mov_b32 m0, s72
	s_addc_u32 s55, s21, s9
	s_add_i32 s73, s68, 0x2000
	v_add_u32_e32 v0, v3, v14
	v_add_lshl_u32 v1, v13, v1, 11
	global_load_lds_dwordx4 v194, s[36:37]
	s_mov_b32 m0, s68
	s_add_u32 s36, s54, 0x40000
	v_lshl_add_u32 v200, v0, 1, v1
	global_load_lds_dwordx4 v198, s[54:55]
	s_mov_b32 m0, s73
	s_addc_u32 s37, s55, 0
	s_add_i32 s74, s68, 0x4000
	global_load_lds_dwordx4 v200, s[54:55]
	s_mov_b32 m0, s74
	s_add_i32 s75, s68, 0x6000
	global_load_lds_dwordx4 v198, s[36:37]
	s_mov_b32 m0, s75
	v_mov_b32_e32 v197, v193
	global_load_lds_dwordx4 v200, s[36:37]
	v_mov_b32_e32 v195, v193
	v_mov_b32_e32 v199, v193
	v_mov_b32_e32 v201, v193
	s_cmp_eq_u32 s18, 1
	v_lshl_add_u64 v[6:7], s[38:39], 0, v[196:197]
	v_lshl_add_u64 v[4:5], s[38:39], 0, v[194:195]
	v_lshl_add_u64 v[0:1], s[54:55], 0, v[198:199]
	s_cselect_b64 s[40:41], -1, 0
	s_cmp_lg_u32 s18, 1
	v_lshl_add_u64 v[2:3], s[54:55], 0, v[200:201]
	s_cbranch_scc1 .LBB0_306
	s_barrier

; #define REP(k) for (int _rep = 0; _rep < (((PROBE_MASK >> (k)) & 1) ? 2 : 1); ++_rep)
; __global__ void __launch_bounds__(NTHR, 2) mk_fwd(Args args) {
;     ...
;             { pg8::ColMapOrder S; S.b.init(NROW, 11 * 256, F.G, F.wg); S.map = 0xCBA98763210ull; pg8::EpiBf16 E{(bf16_t*)(F.ws + WS_U), DIN};
;               REP(1) pg8::gemm_phase<pg8::EpiBf16, pg8::ColMapOrder, false>(F.tid, F.lds, (const bf16_t*)(F.ws + WS_XM), (const bf16_t*)(F.ws + WS_WIN) + (size_t)l * DIN * DM, DM, nullptr, S, E); }
;             __syncthreads(); FRESH();
;             { pg8::ColMapOrder S; S.b.init(NROW, 2 * 256, F.G, (F.wg + 80) % F.G); S.map = 0x54ull; pg8::EpiVT E{(bf16_t*)(F.ws + WS_VT), UV};
;               REP(1) pg8::gemm_phase<pg8::EpiVT, pg8::ColMapOrder, false, false, true, true, false, true>(F.tid, F.lds, (const bf16_t*)(F.ws + WS_XM), (const bf16_t*)(F.ws + WS_WIN) + (size_t)l * DIN * DM, DM, nullptr, S, E); }
;         }
.LBB0_331:
	s_cmp_eq_u32 s100, 1
	s_cbranch_scc0 .Lpa_done
	s_mov_b32 s100, 2
	s_branch .Lpa_body

; __global__ void __launch_bounds__(NTHR, 2) mk_fwd(Args args) {
	.amdhsa_kernel _Z6mk_fwd4Args
		.amdhsa_group_segment_fixed_size 0
		.amdhsa_private_segment_fixed_size 0
		.amdhsa_kernarg_size 568
		.amdhsa_user_sgpr_count 2
		.amdhsa_user_sgpr_dispatch_ptr 0
		.amdhsa_user_sgpr_queue_ptr 0
		.amdhsa_user_sgpr_kernarg_segment_ptr 1
		.amdhsa_user_sgpr_dispatch_id 0
		.amdhsa_user_sgpr_kernarg_preload_length 0
		.amdhsa_user_sgpr_kernarg_preload_offset 0
		.amdhsa_user_sgpr_private_segment_size 0
		.amdhsa_uses_dynamic_stack 0
		.amdhsa_enable_private_segment 0
		.amdhsa_system_sgpr_workgroup_id_x 1
		.amdhsa_system_sgpr_workgroup_id_y 0
		.amdhsa_system_sgpr_workgroup_id_z 0
		.amdhsa_system_sgpr_workgroup_info 0
		.amdhsa_system_vgpr_workitem_id 0
		.amdhsa_next_free_vgpr 256
		.amdhsa_next_free_sgpr 102
		.amdhsa_accum_offset 256
		.amdhsa_reserve_vcc 1
		.amdhsa_float_round_mode_32 0
		.amdhsa_float_round_mode_16_64 0
		.amdhsa_float_denorm_mode_32 3
		.amdhsa_float_denorm_mode_16_64 3
		.amdhsa_dx10_clamp 1
		.amdhsa_ieee_mode 1
		.amdhsa_fp16_overflow 0
		.amdhsa_tg_split 0
		.amdhsa_exception_fp_ieee_invalid_op 0
		.amdhsa_exception_fp_denorm_src 0
		.amdhsa_exception_fp_ieee_div_zero 0
		.amdhsa_exception_fp_ieee_overflow 0
		.amdhsa_exception_fp_ieee_underflow 0
		.amdhsa_exception_fp_ieee_inexact 0
		.amdhsa_exception_int_div_zero 0
	.end_amdhsa_kernel

; __global__ void __launch_bounds__(NTHR, 2) mk_fwd(Args args) {
amdhsa.kernels:
  - .agpr_count:     0
    .args:
      - .offset:         0
        .size:           312
        .value_kind:     by_value
      - .offset:         312
        .size:           4
        .value_kind:     hidden_block_count_x
      - .offset:         316
        .size:           4
        .value_kind:     hidden_block_count_y
      - .offset:         320
        .size:           4
        .value_kind:     hidden_block_count_z
      - .offset:         324
        .size:           2
        .value_kind:     hidden_group_size_x
      - .offset:         326
        .size:           2
        .value_kind:     hidden_group_size_y
      - .offset:         328
        .size:           2
        .value_kind:     hidden_group_size_z
      - .offset:         330
        .size:           2
        .value_kind:     hidden_remainder_x
      - .offset:         332
        .size:           2
        .value_kind:     hidden_remainder_y
      - .offset:         334
        .size:           2
        .value_kind:     hidden_remainder_z
      - .offset:         352
        .size:           8
        .value_kind:     hidden_global_offset_x
      - .offset:         360
        .size:           8
        .value_kind:     hidden_global_offset_y
      - .offset:         368
        .size:           8
        .value_kind:     hidden_global_offset_z
      - .offset:         376
        .size:           2
        .value_kind:     hidden_grid_dims
      - .offset:         432
        .size:           4
        .value_kind:     hidden_dynamic_lds_size
    .group_segment_fixed_size: 0
    .kernarg_segment_align: 8
    .kernarg_segment_size: 568
    .language:       OpenCL C
    .language_version:
      - 2
      - 0
    .max_flat_workgroup_size: 512
    .name:           _Z6mk_fwd4Args
    .private_segment_fixed_size: 0
    .sgpr_count:     108
    .sgpr_spill_count: 231
    .symbol:         _Z6mk_fwd4Args.kd
    .uniform_work_group_size: 1
    .uses_dynamic_stack: false
    .vgpr_count:     256
    .vgpr_spill_count: 0
    .wavefront_size: 64
